# sel tile: first four exps issued in the third score MFMA's shadow (valid when no causal mask and no rescale, else recomputed on the rare paths)
# baseline (speedup 1.0000x reference)
; #define RD16(dst, base, off) asm volatile("ds_read_b128 %0, %1 offset:%2" : "=&v"(dst) : "v"(base), "i"(off) : "memory")
; #define LGKM_W(n) asm volatile("s_waitcnt lgkmcnt(" #n ")" ::: "memory"); SBAR()
; #define QK8_MM(T_) do { i32x8a kf; kf.lo = lo[T_]; kf.hi = hi[T_]; s[T_] = __builtin_amdgcn_mfma_scale_f32_16x16x128_f8f6f4(kf, g.q8, (f32x4){c0, c0, c0, c0}, 0, 0, 0, 0x7f7f7f7f, 0, 0x7c7c7c7c); } while (0)
; __device__ __forceinline__ void qk8_tile_c(f32x4 (&s)[4], const GS8& g, const unsigned kb  , const float c0  ) {
;     i32x4a lo[4], hi[4];
;     RD16(lo[0], kb, 0); RD16(hi[0], kb, 16); RD16(lo[1], kb, 16 * K8ST); RD16(hi[1], kb, 16 * K8ST + 16);
;     RD16(lo[2], kb, 32 * K8ST); RD16(hi[2], kb, 32 * K8ST + 16); RD16(lo[3], kb, 48 * K8ST); RD16(hi[3], kb, 48 * K8ST + 16);
;     ...
;     LGKM_W(6); QK8_MM(0); LGKM_W(4); QK8_MM(1); LGKM_W(2); QK8_MM(2); LGKM_W(0); QK8_MM(3);
;     ...
; }
; template <class G> __device__ __forceinline__ void online_sm8(f32x4 (&s)[4], G& g, const float ref) {
;     ...
;     float ps = 0.f;
; #pragma unroll
;     for (int T_ = 0; T_ < 4; ++T_)
; #pragma unroll
;         for (int i = 0; i < 4; ++i) { s[T_][i] = __builtin_amdgcn_exp2f(s[T_][i]); ps += s[T_][i]; }
.Lsel_nodma:
	s_lshr_b32 s45, s67, s36
	s_and_b32 s97, s45, 0xff
	s_cbranch_scc0 .LBB0_1798
	ds_read_b128 v[84:87], v208 offset:0
	ds_read_b128 v[88:91], v208 offset:16
	ds_read_b128 v[92:95], v208 offset:0x900
	ds_read_b128 v[96:99], v208 offset:0x910
	ds_read_b128 v[118:121], v208 offset:0x1200
	ds_read_b128 v[122:125], v208 offset:0x1210
	s_and_b32 vcc_lo, s45, 15
	s_cbranch_scc0 .Lsel_g1_pre
	v_and_b32_e32 v18, s45, v154
	v_cmp_eq_u32_e32 vcc, 0, v18
	s_lshr_b32 s44, s66, s36
	s_and_b32 s44, s44, 0xff
	v_cndmask_b32_e32 v210, v216, v181, vcc
	v_mov_b32_e32 v211, v210
	v_mov_b32_e32 v212, v210
	v_mov_b32_e32 v213, v210
	ds_read_b128 v[126:129], v208 offset:0x1b00
	ds_read_b128 v[130:133], v208 offset:0x1b10
	s_waitcnt lgkmcnt(6)
	v_mfma_scale_f32_16x16x128_f8f6f4 v[84:87], v[84:91], v[0:7], v[210:213], v178, v177 op_sel_hi:[0,0,0]
	ds_read_b64 v[148:149], v207 offset:0
	ds_read_b64 v[146:147], v207 offset:32
	ds_read_b64 v[144:145], v207 offset:0x500
	ds_read_b64 v[142:143], v207 offset:0x520
	ds_read_b64 v[140:141], v207 offset:0xa00
	ds_read_b64 v[136:137], v207 offset:0xa20
	ds_read_b64 v[138:139], v207 offset:0xf00
	ds_read_b64 v[134:135], v207 offset:0xf20
	s_waitcnt lgkmcnt(12)
	v_mfma_scale_f32_16x16x128_f8f6f4 v[88:91], v[92:99], v[0:7], v[210:213], v178, v177 op_sel_hi:[0,0,0]
	s_waitcnt lgkmcnt(10)
	v_mfma_scale_f32_16x16x128_f8f6f4 v[92:95], v[118:125], v[0:7], v[210:213], v178, v177 op_sel_hi:[0,0,0]
	v_exp_f32_e32 v240, v84
	v_exp_f32_e32 v241, v85
	v_exp_f32_e32 v242, v86
	v_exp_f32_e32 v243, v87
	s_waitcnt lgkmcnt(8)
	s_cmp_eq_u32 s44, s58
	v_mfma_scale_f32_16x16x128_f8f6f4 v[96:99], v[126:133], v[0:7], v[210:213], v178, v177 op_sel_hi:[0,0,0]
	ds_read_b64 v[132:133], v207 offset:0x1400
	ds_read_b64 v[130:131], v207 offset:0x1420
	ds_read_b64 v[128:129], v207 offset:0x1900
	ds_read_b64 v[126:127], v207 offset:0x1920
	ds_read_b64 v[124:125], v207 offset:0x1e00
	ds_read_b64 v[118:119], v207 offset:0x2300
	s_cbranch_scc1 .Lsel_diag_g0

; __device__ __forceinline__ unsigned pk4_fp8(float a, float b, float c, float d) { unsigned w = 0u; w = __builtin_amdgcn_cvt_pk_fp8_f32(a, b, w, false); w = __builtin_amdgcn_cvt_pk_fp8_f32(c, d, w, true); return w; }
; #define LGKM_W(n) asm volatile("s_waitcnt lgkmcnt(" #n ")" ::: "memory"); SBAR()
; #define PV8_MM(dt) do { g.o[dt] = __builtin_amdgcn_mfma_f32_16x16x32_fp8_fp8(f.a[dt][0], b0, g.o[dt], 0, 0, 0); g.o[dt] = __builtin_amdgcn_mfma_f32_16x16x32_fp8_fp8(f.a[dt][1], b1, g.o[dt], 0, 0, 0); } while (0)
; template <class G> __device__ __forceinline__ void pv8_mm(G& g, const f32x4 (&s)[4], const VT8Frag& f) {
;     ...
;     unsigned pa[4];
; #pragma unroll
;     for (int T_ = 0; T_ < 4; ++T_) pa[T_] = pk4_fp8(s[T_][0], s[T_][1], s[T_][2], s[T_][3]);
;     const long b0 = (long)(((unsigned long long)pa[1] << 32) | pa[0]), b1 = (long)(((unsigned long long)pa[3] << 32) | pa[2]);
;     LGKM_W(14); PV8_MM(0); LGKM_W(12); PV8_MM(1); LGKM_W(10); PV8_MM(2); LGKM_W(8); PV8_MM(3);
;     LGKM_W(6); PV8_MM(4); LGKM_W(4); PV8_MM(5); LGKM_W(2); PV8_MM(6); LGKM_W(0); PV8_MM(7);
;     ...
; }
; template <class G> __device__ __forceinline__ void online_sm8(f32x4 (&s)[4], G& g, const float ref) {
;     ...
;     float ps = 0.f;
; #pragma unroll
;     for (int T_ = 0; T_ < 4; ++T_)
; #pragma unroll
;         for (int i = 0; i < 4; ++i) { s[T_][i] = __builtin_amdgcn_exp2f(s[T_][i]); ps += s[T_][i]; }
;     g.l += ps;
.Lsel_pvs_g0:
	ds_read_b64 v[120:121], v207 offset:0x1e20
	ds_read_b64 v[122:123], v207 offset:0x2320
	v_exp_f32_e32 v244, v88
	v_exp_f32_e32 v245, v89
	v_exp_f32_e32 v246, v90
	v_exp_f32_e32 v247, v91
	s_waitcnt lgkmcnt(2)
	v_cvt_pk_fp8_f32 v84, v240, v241
	v_cvt_pk_fp8_f32 v85, v244, v245
	v_cvt_pk_fp8_f32 v84, v242, v243 op_sel:[0,0,1]
	v_cvt_pk_fp8_f32 v85, v246, v247 op_sel:[0,0,1]
	v_exp_f32_e32 v248, v92
	v_exp_f32_e32 v249, v93
	v_mfma_f32_16x16x32_fp8_fp8 v[80:83], v[148:149], v[84:85], v[80:83]
	v_exp_f32_e32 v250, v94
	v_mfma_f32_16x16x32_fp8_fp8 v[76:79], v[144:145], v[84:85], v[76:79]
	v_exp_f32_e32 v251, v95
	v_mfma_f32_16x16x32_fp8_fp8 v[72:75], v[140:141], v[84:85], v[72:75]
	v_exp_f32_e32 v252, v96
	v_mfma_f32_16x16x32_fp8_fp8 v[68:71], v[138:139], v[84:85], v[68:71]
	v_exp_f32_e32 v253, v97
	v_mfma_f32_16x16x32_fp8_fp8 v[64:67], v[132:133], v[84:85], v[64:67]
	v_exp_f32_e32 v254, v98
	v_mfma_f32_16x16x32_fp8_fp8 v[60:63], v[128:129], v[84:85], v[60:63]
	v_exp_f32_e32 v255, v99
	v_mfma_f32_16x16x32_fp8_fp8 v[56:59], v[124:125], v[84:85], v[56:59]
	v_mfma_f32_16x16x32_fp8_fp8 v[52:55], v[118:119], v[84:85], v[52:55]
	s_waitcnt lgkmcnt(0)
	v_cvt_pk_fp8_f32 v86, v248, v249
	v_cvt_pk_fp8_f32 v87, v252, v253
	v_cvt_pk_fp8_f32 v86, v250, v251 op_sel:[0,0,1]
	v_cvt_pk_fp8_f32 v87, v254, v255 op_sel:[0,0,1]
	v_add_f32_e32 v240, v240, v241
	v_add_f32_e32 v242, v242, v243
	v_mfma_f32_16x16x32_fp8_fp8 v[80:83], v[146:147], v[86:87], v[80:83]
	v_add_f32_e32 v244, v244, v245
	v_add_f32_e32 v246, v246, v247
	v_mfma_f32_16x16x32_fp8_fp8 v[76:79], v[142:143], v[86:87], v[76:79]
	v_add_f32_e32 v248, v248, v249
	v_add_f32_e32 v250, v250, v251
	v_mfma_f32_16x16x32_fp8_fp8 v[72:75], v[136:137], v[86:87], v[72:75]
	v_add_f32_e32 v252, v252, v253
	v_add_f32_e32 v254, v254, v255
	v_mfma_f32_16x16x32_fp8_fp8 v[68:71], v[134:135], v[86:87], v[68:71]
	v_add_f32_e32 v240, v240, v242
	v_add_f32_e32 v244, v244, v246
	v_mfma_f32_16x16x32_fp8_fp8 v[64:67], v[130:131], v[86:87], v[64:67]
	v_add_f32_e32 v248, v248, v250
	v_add_f32_e32 v252, v252, v254
	v_mfma_f32_16x16x32_fp8_fp8 v[60:63], v[126:127], v[86:87], v[60:63]
	v_add_f32_e32 v240, v240, v244
	v_add_f32_e32 v248, v248, v252
	v_mfma_f32_16x16x32_fp8_fp8 v[56:59], v[120:121], v[86:87], v[56:59]
	v_add_f32_e32 v240, v240, v248
	v_add_f32_e32 v183, v183, v240
	v_mfma_f32_16x16x32_fp8_fp8 v[52:55], v[122:123], v[86:87], v[52:55]

; #define RD16(dst, base, off) asm volatile("ds_read_b128 %0, %1 offset:%2" : "=&v"(dst) : "v"(base), "i"(off) : "memory")
; #define LGKM_W(n) asm volatile("s_waitcnt lgkmcnt(" #n ")" ::: "memory"); SBAR()
; #define QK8_MM(T_) do { i32x8a kf; kf.lo = lo[T_]; kf.hi = hi[T_]; s[T_] = __builtin_amdgcn_mfma_scale_f32_16x16x128_f8f6f4(kf, g.q8, (f32x4){c0, c0, c0, c0}, 0, 0, 0, 0x7f7f7f7f, 0, 0x7c7c7c7c); } while (0)
; __device__ __forceinline__ void qk8_tile_c(f32x4 (&s)[4], const GS8& g, const unsigned kb  , const float c0  ) {
;     i32x4a lo[4], hi[4];
;     RD16(lo[0], kb, 0); RD16(hi[0], kb, 16); RD16(lo[1], kb, 16 * K8ST); RD16(hi[1], kb, 16 * K8ST + 16);
;     RD16(lo[2], kb, 32 * K8ST); RD16(hi[2], kb, 32 * K8ST + 16); RD16(lo[3], kb, 48 * K8ST); RD16(hi[3], kb, 48 * K8ST + 16);
;     ...
;     LGKM_W(6); QK8_MM(0); LGKM_W(4); QK8_MM(1); LGKM_W(2); QK8_MM(2); LGKM_W(0); QK8_MM(3);
;     ...
; }
; template <class G> __device__ __forceinline__ void online_sm8(f32x4 (&s)[4], G& g, const float ref) {
;     ...
;     float ps = 0.f;
; #pragma unroll
;     for (int T_ = 0; T_ < 4; ++T_)
; #pragma unroll
;         for (int i = 0; i < 4; ++i) { s[T_][i] = __builtin_amdgcn_exp2f(s[T_][i]); ps += s[T_][i]; }
.Lsel_g1_pre:
	s_lshr_b32 s45, s45, 4
	v_and_b32_e32 v18, s45, v154
	v_cmp_eq_u32_e32 vcc, 0, v18
	s_lshr_b32 s44, s66, s36
	s_and_b32 s44, s44, 0xff
	v_cndmask_b32_e32 v210, v220, v181, vcc
	v_mov_b32_e32 v211, v210
	v_mov_b32_e32 v212, v210
	v_mov_b32_e32 v213, v210
	ds_read_b128 v[126:129], v208 offset:0x1b00
	ds_read_b128 v[130:133], v208 offset:0x1b10
	s_waitcnt lgkmcnt(6)
	v_mfma_scale_f32_16x16x128_f8f6f4 v[84:87], v[84:91], v[8:15], v[210:213], v178, v177 op_sel_hi:[0,0,0]
	ds_read_b64 v[148:149], v207 offset:0
	ds_read_b64 v[146:147], v207 offset:32
	ds_read_b64 v[144:145], v207 offset:0x500
	ds_read_b64 v[142:143], v207 offset:0x520
	ds_read_b64 v[140:141], v207 offset:0xa00
	ds_read_b64 v[136:137], v207 offset:0xa20
	ds_read_b64 v[138:139], v207 offset:0xf00
	ds_read_b64 v[134:135], v207 offset:0xf20
	s_waitcnt lgkmcnt(12)
	v_mfma_scale_f32_16x16x128_f8f6f4 v[88:91], v[92:99], v[8:15], v[210:213], v178, v177 op_sel_hi:[0,0,0]
	s_waitcnt lgkmcnt(10)
	v_mfma_scale_f32_16x16x128_f8f6f4 v[92:95], v[118:125], v[8:15], v[210:213], v178, v177 op_sel_hi:[0,0,0]
	v_exp_f32_e32 v240, v84
	v_exp_f32_e32 v241, v85
	v_exp_f32_e32 v242, v86
	v_exp_f32_e32 v243, v87
	s_waitcnt lgkmcnt(8)
	s_cmp_eq_u32 s44, s58
	v_mfma_scale_f32_16x16x128_f8f6f4 v[96:99], v[126:133], v[8:15], v[210:213], v178, v177 op_sel_hi:[0,0,0]
	ds_read_b64 v[132:133], v207 offset:0x1400
	ds_read_b64 v[130:131], v207 offset:0x1420
	ds_read_b64 v[128:129], v207 offset:0x1900
	ds_read_b64 v[126:127], v207 offset:0x1920
	ds_read_b64 v[124:125], v207 offset:0x1e00
	ds_read_b64 v[118:119], v207 offset:0x2300
	s_cbranch_scc1 .Lsel_diag_g1

; __device__ __forceinline__ unsigned pk4_fp8(float a, float b, float c, float d) { unsigned w = 0u; w = __builtin_amdgcn_cvt_pk_fp8_f32(a, b, w, false); w = __builtin_amdgcn_cvt_pk_fp8_f32(c, d, w, true); return w; }
; #define LGKM_W(n) asm volatile("s_waitcnt lgkmcnt(" #n ")" ::: "memory"); SBAR()
; #define PV8_MM(dt) do { g.o[dt] = __builtin_amdgcn_mfma_f32_16x16x32_fp8_fp8(f.a[dt][0], b0, g.o[dt], 0, 0, 0); g.o[dt] = __builtin_amdgcn_mfma_f32_16x16x32_fp8_fp8(f.a[dt][1], b1, g.o[dt], 0, 0, 0); } while (0)
; __device__ __forceinline__ void mask_scores(f32x4 (&s)[4], int a, unsigned W, int kb, int q4) {
;     const float NEG = -__builtin_inff();
; #pragma unroll
;     for (int T_ = 0; T_ < 4; ++T_)
; #pragma unroll
;         for (int i = 0; i < 4; ++i) if ((unsigned)(a - (kb + 16 * T_ + 4 * q4 + i)) >= W) s[T_][i] = NEG;
; }
; template <class G> __device__ __forceinline__ void pv8_mm(G& g, const f32x4 (&s)[4], const VT8Frag& f) {
;     ...
;     unsigned pa[4];
; #pragma unroll
;     for (int T_ = 0; T_ < 4; ++T_) pa[T_] = pk4_fp8(s[T_][0], s[T_][1], s[T_][2], s[T_][3]);
;     const long b0 = (long)(((unsigned long long)pa[1] << 32) | pa[0]), b1 = (long)(((unsigned long long)pa[3] << 32) | pa[2]);
;     LGKM_W(14); PV8_MM(0); LGKM_W(12); PV8_MM(1); LGKM_W(10); PV8_MM(2); LGKM_W(8); PV8_MM(3);
;     LGKM_W(6); PV8_MM(4); LGKM_W(4); PV8_MM(5); LGKM_W(2); PV8_MM(6); LGKM_W(0); PV8_MM(7);
;     ...
; }
.Lsel_pvs_g1:
	ds_read_b64 v[120:121], v207 offset:0x1e20
	ds_read_b64 v[122:123], v207 offset:0x2320
	v_exp_f32_e32 v244, v88
	v_exp_f32_e32 v245, v89
	v_exp_f32_e32 v246, v90
	v_exp_f32_e32 v247, v91
	s_waitcnt lgkmcnt(2)
	v_cvt_pk_fp8_f32 v84, v240, v241
	v_cvt_pk_fp8_f32 v85, v244, v245
	v_cvt_pk_fp8_f32 v84, v242, v243 op_sel:[0,0,1]
	v_cvt_pk_fp8_f32 v85, v246, v247 op_sel:[0,0,1]
	v_exp_f32_e32 v248, v92
	v_exp_f32_e32 v249, v93
	v_mfma_f32_16x16x32_fp8_fp8 v[48:51], v[148:149], v[84:85], v[48:51]
	v_exp_f32_e32 v250, v94
	v_mfma_f32_16x16x32_fp8_fp8 v[44:47], v[144:145], v[84:85], v[44:47]
	v_exp_f32_e32 v251, v95
	v_mfma_f32_16x16x32_fp8_fp8 v[40:43], v[140:141], v[84:85], v[40:43]
	v_exp_f32_e32 v252, v96
	v_mfma_f32_16x16x32_fp8_fp8 v[36:39], v[138:139], v[84:85], v[36:39]
	v_exp_f32_e32 v253, v97
	v_mfma_f32_16x16x32_fp8_fp8 v[32:35], v[132:133], v[84:85], v[32:35]
	v_exp_f32_e32 v254, v98
	v_mfma_f32_16x16x32_fp8_fp8 v[28:31], v[128:129], v[84:85], v[28:31]
	v_exp_f32_e32 v255, v99
	v_mfma_f32_16x16x32_fp8_fp8 v[24:27], v[124:125], v[84:85], v[24:27]
	v_mfma_f32_16x16x32_fp8_fp8 v[20:23], v[118:119], v[84:85], v[20:23]
	s_waitcnt lgkmcnt(0)
	v_cvt_pk_fp8_f32 v86, v248, v249
	v_cvt_pk_fp8_f32 v87, v252, v253
	v_cvt_pk_fp8_f32 v86, v250, v251 op_sel:[0,0,1]
	v_cvt_pk_fp8_f32 v87, v254, v255 op_sel:[0,0,1]
	v_add_f32_e32 v240, v240, v241
	v_add_f32_e32 v242, v242, v243
	v_mfma_f32_16x16x32_fp8_fp8 v[48:51], v[146:147], v[86:87], v[48:51]
	v_add_f32_e32 v244, v244, v245
	v_add_f32_e32 v246, v246, v247
	v_mfma_f32_16x16x32_fp8_fp8 v[44:47], v[142:143], v[86:87], v[44:47]
	v_add_f32_e32 v248, v248, v249
	v_add_f32_e32 v250, v250, v251
	v_mfma_f32_16x16x32_fp8_fp8 v[40:43], v[136:137], v[86:87], v[40:43]
	v_add_f32_e32 v252, v252, v253
	v_add_f32_e32 v254, v254, v255
	v_mfma_f32_16x16x32_fp8_fp8 v[36:39], v[134:135], v[86:87], v[36:39]
	v_add_f32_e32 v240, v240, v242
	v_add_f32_e32 v244, v244, v246
	v_mfma_f32_16x16x32_fp8_fp8 v[32:35], v[130:131], v[86:87], v[32:35]
	v_add_f32_e32 v248, v248, v250
	v_add_f32_e32 v252, v252, v254
	v_mfma_f32_16x16x32_fp8_fp8 v[28:31], v[126:127], v[86:87], v[28:31]
	v_add_f32_e32 v240, v240, v244
	v_add_f32_e32 v248, v248, v252
	v_mfma_f32_16x16x32_fp8_fp8 v[24:27], v[120:121], v[86:87], v[24:27]
	v_add_f32_e32 v240, v240, v248
	v_add_f32_e32 v182, v182, v240
	v_mfma_f32_16x16x32_fp8_fp8 v[20:23], v[122:123], v[86:87], v[20:23]
	s_branch .LBB0_1798
.LBB0_1808:
	v_exp_f32_e32 v240, v84
	v_exp_f32_e32 v241, v85
	v_exp_f32_e32 v242, v86
	v_exp_f32_e32 v243, v87
	s_branch .Lsel_pvs_g0
.Lsel_diag_g0:
	s_lshl_b32 s12, s44, 6
	v_add_u32_e32 v18, s12, v155
	v_sub_u32_e32 v114, s55, v18
	v_cmp_gt_u32_e32 vcc, 2.0, v114
	v_sub_u32_e32 v114, v18, v16
	s_nop 2
	v_cndmask_b32_e32 v84, v181, v84, vcc
	v_cmp_lt_u32_e32 vcc, s91, v114
	v_sub_u32_e32 v114, v184, v18
	s_nop 0
	v_cndmask_b32_e32 v85, v181, v85, vcc
	v_cmp_gt_u32_e32 vcc, 2.0, v114
	v_sub_u32_e32 v114, v185, v18
	s_nop 0
	v_cndmask_b32_e32 v86, v181, v86, vcc
	v_cmp_gt_u32_e32 vcc, 2.0, v114
	v_sub_u32_e32 v114, s68, v18
	s_nop 0
	v_cndmask_b32_e32 v87, v181, v87, vcc
	v_cmp_gt_u32_e32 vcc, 2.0, v114
	v_sub_u32_e32 v114, v186, v18
	s_nop 0
	v_cndmask_b32_e32 v88, v181, v88, vcc
	v_cmp_gt_u32_e32 vcc, 2.0, v114
	v_sub_u32_e32 v114, v187, v18
	s_nop 0
	v_cndmask_b32_e32 v89, v181, v89, vcc
	v_cmp_gt_u32_e32 vcc, 2.0, v114
	v_sub_u32_e32 v114, v188, v18
	s_nop 0
	v_cndmask_b32_e32 v90, v181, v90, vcc
	v_cmp_gt_u32_e32 vcc, 2.0, v114
	v_sub_u32_e32 v114, s69, v18
	s_nop 0
	v_cndmask_b32_e32 v91, v181, v91, vcc
	v_cmp_gt_u32_e32 vcc, 2.0, v114
	v_sub_u32_e32 v114, v189, v18
	s_nop 0
	v_cndmask_b32_e32 v92, v181, v92, vcc
	v_cmp_gt_u32_e32 vcc, 2.0, v114
	v_sub_u32_e32 v114, v190, v18
	s_nop 0
	v_cndmask_b32_e32 v93, v181, v93, vcc
	v_cmp_gt_u32_e32 vcc, 2.0, v114
	v_sub_u32_e32 v114, v191, v18
	s_nop 0
	v_cndmask_b32_e32 v94, v181, v94, vcc
	v_cmp_gt_u32_e32 vcc, 2.0, v114
	v_sub_u32_e32 v114, s70, v18
	s_nop 0
	v_cndmask_b32_e32 v95, v181, v95, vcc
	v_cmp_gt_u32_e32 vcc, 2.0, v114
	v_sub_u32_e32 v114, v192, v18
	s_nop 0
	v_cndmask_b32_e32 v96, v181, v96, vcc
	v_cmp_gt_u32_e32 vcc, 2.0, v114
	v_sub_u32_e32 v114, v193, v18
	v_sub_u32_e32 v18, v194, v18
	v_cndmask_b32_e32 v97, v181, v97, vcc
	v_cmp_gt_u32_e32 vcc, 2.0, v114
	s_nop 1
	v_cndmask_b32_e32 v98, v181, v98, vcc
	v_cmp_gt_u32_e32 vcc, 2.0, v18
	s_nop 1
	v_cndmask_b32_e32 v99, v181, v99, vcc
	v_max_f32_e32 v18, v84, v85
	v_max3_f32 v18, v18, v86, v87
	v_max3_f32 v18, v18, v88, v89
	v_max3_f32 v18, v18, v90, v91
	v_max3_f32 v18, v18, v92, v93
	v_max3_f32 v18, v18, v94, v95
	v_max3_f32 v18, v18, v96, v97
	v_max3_f32 v114, v18, v98, v99
	v_add_f32_e32 v150, v217, v114
	v_cmp_le_f32_e32 vcc, v150, v218
	s_cmp_eq_u64 vcc, exec
	s_cbranch_scc0 .Lsel_resc_g0
	s_branch .LBB0_1808

; __device__ __forceinline__ float xmax16(float v) { float a = v, b = v; PL_SWAP16(a, b); return fmaxf(a, b); }
; __device__ __forceinline__ float xmax32(float v) { float a = v, b = v; PL_SWAP32(a, b); return fmaxf(a, b); }
; __device__ __forceinline__ void mask_scores(f32x4 (&s)[4], int a, unsigned W, int kb, int q4) {
;     const float NEG = -__builtin_inff();
; #pragma unroll
;     for (int T_ = 0; T_ < 4; ++T_)
; #pragma unroll
;         for (int i = 0; i < 4; ++i) if ((unsigned)(a - (kb + 16 * T_ + 4 * q4 + i)) >= W) s[T_][i] = NEG;
; }
; template <class G> __device__ __forceinline__ void online_sm8(f32x4 (&s)[4], G& g, const float ref) {
;     float mx = s[0][0];
; #pragma unroll
;     for (int T_ = 0; T_ < 4; ++T_)
; #pragma unroll
;         for (int i = 0; i < 4; ++i) mx = fmaxf(mx, s[T_][i]);
;     const float t = mx + (ref - 5.f);
;     if (!__all(t <= g.m + SM_THR8)) {
;         const float mr = xmax32(xmax16(t));
;         const float mn = fmaxf(g.m, mr); const float al = __builtin_amdgcn_exp2f(g.m - mn); g.m = mn; g.l *= al;
.Lsel_diag_g1:
	s_lshl_b32 s12, s44, 6
	v_add_u32_e32 v114, s12, v155
	v_sub_u32_e32 v116, v195, v114
	v_cmp_gt_u32_e32 vcc, 2.0, v116
	v_sub_u32_e32 v116, v114, v195
	s_nop 2
	v_cndmask_b32_e32 v84, v181, v84, vcc
	v_cmp_lt_u32_e32 vcc, s91, v116
	v_sub_u32_e32 v116, v196, v114
	s_nop 0
	v_cndmask_b32_e32 v85, v181, v85, vcc
	v_cmp_gt_u32_e32 vcc, 2.0, v116
	v_sub_u32_e32 v116, v197, v114
	s_nop 0
	v_cndmask_b32_e32 v86, v181, v86, vcc
	v_cmp_gt_u32_e32 vcc, 2.0, v116
	v_sub_u32_e32 v116, s71, v114
	s_nop 0
	v_cndmask_b32_e32 v87, v181, v87, vcc
	v_cmp_gt_u32_e32 vcc, 2.0, v116
	v_sub_u32_e32 v116, v198, v114
	s_nop 0
	v_cndmask_b32_e32 v88, v181, v88, vcc
	v_cmp_gt_u32_e32 vcc, 2.0, v116
	v_sub_u32_e32 v116, v199, v114
	s_nop 0
	v_cndmask_b32_e32 v89, v181, v89, vcc
	v_cmp_gt_u32_e32 vcc, 2.0, v116
	v_sub_u32_e32 v116, v200, v114
	s_nop 0
	v_cndmask_b32_e32 v90, v181, v90, vcc
	v_cmp_gt_u32_e32 vcc, 2.0, v116
	v_sub_u32_e32 v116, s72, v114
	s_nop 0
	v_cndmask_b32_e32 v91, v181, v91, vcc
	v_cmp_gt_u32_e32 vcc, 2.0, v116
	v_sub_u32_e32 v116, v201, v114
	s_nop 0
	v_cndmask_b32_e32 v92, v181, v92, vcc
	v_cmp_gt_u32_e32 vcc, 2.0, v116
	v_sub_u32_e32 v116, v202, v114
	s_nop 0
	v_cndmask_b32_e32 v93, v181, v93, vcc
	v_cmp_gt_u32_e32 vcc, 2.0, v116
	v_sub_u32_e32 v116, v203, v114
	s_nop 0
	v_cndmask_b32_e32 v94, v181, v94, vcc
	v_cmp_gt_u32_e32 vcc, 2.0, v116
	v_sub_u32_e32 v116, s73, v114
	s_nop 0
	v_cndmask_b32_e32 v95, v181, v95, vcc
	v_cmp_gt_u32_e32 vcc, 2.0, v116
	v_sub_u32_e32 v116, v204, v114
	s_nop 0
	v_cndmask_b32_e32 v96, v181, v96, vcc
	v_cmp_gt_u32_e32 vcc, 2.0, v116
	v_sub_u32_e32 v116, v205, v114
	v_sub_u32_e32 v114, v206, v114
	v_cndmask_b32_e32 v97, v181, v97, vcc
	v_cmp_gt_u32_e32 vcc, 2.0, v116
	s_nop 1
	v_cndmask_b32_e32 v98, v181, v98, vcc
	v_cmp_gt_u32_e32 vcc, 2.0, v114
	s_nop 1
	v_cndmask_b32_e32 v99, v181, v99, vcc
	v_max_f32_e32 v114, v84, v85
	v_max3_f32 v114, v114, v86, v87
	v_max3_f32 v114, v114, v88, v89
	v_max3_f32 v114, v114, v90, v91
	v_max3_f32 v114, v114, v92, v93
	v_max3_f32 v114, v114, v94, v95
	v_max3_f32 v114, v114, v96, v97
	v_max3_f32 v114, v114, v98, v99
	v_add_f32_e32 v150, v221, v114
	v_cmp_le_f32_e32 vcc, v150, v222
	s_cmp_eq_u64 vcc, exec
	s_cbranch_scc0 .Lsel_resc_g1
	s_branch .LBB0_1797
